# attention swap also in the bitmask body second half-step (temp v179 renamed so finishSM live-out survives)
# baseline (speedup 1.0000x reference)
.LBB0_1147:
	s_waitcnt lgkmcnt(0)
	s_barrier
	v_readlane_b32 vcc_lo, v255, 63
	s_bitcmp1_b32 vcc_lo, 0
	s_cbranch_scc1 .Lsw2_B
.Lsw2_A:
	v_cvt_f32_i32_e32 v99, v216
	v_lshrrev_b32_e32 v115, v208, v196
	v_and_b32_e32 v98, 1, v115
	v_cmp_eq_u32_e32 vcc, 1, v98
	v_mul_f32_e64 v114, -v178, v99
	v_fma_f32 v100, 0, v178, v114
	v_cndmask_b32_e32 v98, v243, v100, vcc
	v_and_b32_e32 v100, 2, v115
	v_fma_f32 v99, -v178, v99, v178
	v_cmp_ne_u32_e32 vcc, 0, v100
	v_and_b32_e32 v102, 8, v115
	v_pk_fma_f32 v[100:101], v[188:189], s[60:61], v[114:115] op_sel_hi:[1,1,0]
	v_cndmask_b32_e32 v99, v243, v99, vcc
	v_and_b32_e32 v103, 4, v115
	v_cmp_ne_u32_e32 vcc, 0, v102
	v_and_b32_e32 v104, 0x200, v115
	v_and_b32_e32 v105, 0x100, v115
	v_cndmask_b32_e32 v101, v243, v101, vcc
	v_cmp_ne_u32_e32 vcc, 0, v103
	v_pk_fma_f32 v[102:103], v[188:189], s[74:75], v[114:115] op_sel_hi:[1,1,0]
	v_and_b32_e32 v106, 0x800, v115
	v_cndmask_b32_e32 v100, v243, v100, vcc
	v_cmp_ne_u32_e32 vcc, 0, v104
	v_and_b32_e32 v107, 0x400, v115
	v_and_b32_e32 v108, 0x20000, v115
	v_cndmask_b32_e32 v103, v243, v103, vcc
	v_cmp_ne_u32_e32 vcc, 0, v105
	v_pk_fma_f32 v[104:105], v[188:189], s[62:63], v[114:115] op_sel_hi:[1,1,0]
	v_and_b32_e32 v109, 0x10000, v115
	v_cndmask_b32_e32 v102, v243, v102, vcc
	v_cmp_ne_u32_e32 vcc, 0, v106
	s_mov_b32 s4, 0x41900000
	s_mov_b32 s5, 0x41980000
	v_cndmask_b32_e32 v105, v243, v105, vcc
	v_cmp_ne_u32_e32 vcc, 0, v107
	v_pk_fma_f32 v[106:107], v[188:189], s[58:59], v[114:115] op_sel_hi:[1,1,0]
	v_and_b32_e32 v110, 0x80000, v115
	v_cndmask_b32_e32 v104, v243, v104, vcc
	v_cmp_ne_u32_e32 vcc, 0, v108
	v_and_b32_e32 v111, 0x40000, v115
	v_and_b32_e32 v112, 0x2000000, v115
	v_cndmask_b32_e32 v107, v243, v107, vcc
	v_cmp_ne_u32_e32 vcc, 0, v109
	v_pk_fma_f32 v[108:109], v[188:189], s[4:5], v[114:115] op_sel_hi:[1,1,0]
	s_mov_b32 s4, 0x41c00000
	v_cndmask_b32_e32 v106, v243, v106, vcc
	v_cmp_ne_u32_e32 vcc, 0, v110
	s_mov_b32 s5, 0x41c80000
	v_and_b32_e32 v113, 0x1000000, v115
	v_cndmask_b32_e32 v109, v243, v109, vcc
	v_cmp_ne_u32_e32 vcc, 0, v111
	v_pk_fma_f32 v[110:111], v[188:189], s[4:5], v[114:115] op_sel_hi:[1,1,0]
	s_mov_b32 s4, 0x41d00000
	v_cndmask_b32_e32 v108, v243, v108, vcc
	v_cmp_ne_u32_e32 vcc, 0, v112
	s_mov_b32 s5, 0x41d80000
	v_and_b32_e32 v116, 0x8000000, v115
	v_cndmask_b32_e32 v111, v243, v111, vcc
	v_cmp_ne_u32_e32 vcc, 0, v113
	v_lshrrev_b32_e32 v223, v208, v197
	v_pk_fma_f32 v[112:113], v[188:189], s[4:5], v[114:115] op_sel_hi:[1,1,0]
	v_cndmask_b32_e32 v110, v243, v110, vcc
	v_and_b32_e32 v115, 0x4000000, v115
	v_cmp_ne_u32_e32 vcc, 0, v116
	v_mov_b32_e32 v230, v178
	v_mov_b32_e32 v231, v178
	v_pk_fma_f32 v[116:117], v[230:231], s[86:87], v[114:115] op_sel_hi:[1,1,0]
	v_cndmask_b32_e32 v113, v243, v113, vcc
	v_cmp_ne_u32_e32 vcc, 0, v115
	v_pk_fma_f32 v[118:119], v[230:231], s[88:89], v[114:115] op_sel_hi:[1,1,0]
	v_pk_fma_f32 v[120:121], v[230:231], s[90:91], v[114:115] op_sel_hi:[1,1,0]
	v_pk_fma_f32 v[122:123], v[230:231], s[92:93], v[114:115] op_sel_hi:[1,1,0]
	v_pk_fma_f32 v[124:125], v[230:231], s[94:95], v[114:115] op_sel_hi:[1,1,0]
	v_pk_fma_f32 v[126:127], v[230:231], s[96:97], v[114:115] op_sel_hi:[1,1,0]
	v_pk_fma_f32 v[128:129], v[230:231], s[68:69], v[114:115] op_sel_hi:[1,1,0]
	v_and_b32_e32 v232, 0x8000000, v223
	v_cndmask_b32_e32 v112, v243, v112, vcc
	v_cmp_ne_u32_e32 vcc, 0, v232
	v_and_b32_e32 v232, 0x4000000, v223
	s_mov_b32 s4, 0x42000000
	v_cndmask_b32_e32 v129, v243, v129, vcc
	v_cmp_ne_u32_e32 vcc, 0, v232
	v_and_b32_e32 v232, 0x2000000, v223
	s_mov_b32 s5, 0x42040000
	v_cndmask_b32_e32 v128, v243, v128, vcc
	v_cmp_ne_u32_e32 vcc, 0, v232
	v_and_b32_e32 v232, 0x1000000, v223
	v_pk_fma_f32 v[114:115], v[184:185], s[4:5], v[114:115] op_sel_hi:[1,1,0]
	v_cndmask_b32_e32 v127, v243, v127, vcc
	v_cmp_ne_u32_e32 vcc, 0, v232
	v_and_b32_e32 v232, 0x80000, v223
	s_nop 0
	v_cndmask_b32_e32 v126, v243, v126, vcc
	v_cmp_ne_u32_e32 vcc, 0, v232
	v_and_b32_e32 v232, 0x40000, v223
	s_nop 0
	v_cndmask_b32_e32 v125, v243, v125, vcc
	v_cmp_ne_u32_e32 vcc, 0, v232
	v_and_b32_e32 v232, 0x20000, v223
	s_nop 0
	v_cndmask_b32_e32 v124, v243, v124, vcc
	v_cmp_ne_u32_e32 vcc, 0, v232
	v_and_b32_e32 v232, 0x10000, v223
	s_nop 0
	v_cndmask_b32_e32 v123, v243, v123, vcc
	v_cmp_ne_u32_e32 vcc, 0, v232
	v_and_b32_e32 v232, 0x800, v223
	s_nop 0
	v_cndmask_b32_e32 v122, v243, v122, vcc
	v_cmp_ne_u32_e32 vcc, 0, v232
	v_and_b32_e32 v232, 0x400, v223
	s_nop 0
	v_cndmask_b32_e32 v121, v243, v121, vcc
	v_cmp_ne_u32_e32 vcc, 0, v232
	v_and_b32_e32 v232, 0x200, v223
	s_nop 0
	v_cndmask_b32_e32 v120, v243, v120, vcc
	v_cmp_ne_u32_e32 vcc, 0, v232
	v_and_b32_e32 v232, 0x100, v223
	s_nop 0
	v_cndmask_b32_e32 v119, v243, v119, vcc
	v_cmp_ne_u32_e32 vcc, 0, v232
	v_and_b32_e32 v232, 8, v223
	s_nop 0
	v_cndmask_b32_e32 v118, v243, v118, vcc
	v_cmp_ne_u32_e32 vcc, 0, v232
	v_and_b32_e32 v232, 4, v223
	s_nop 0
	v_cndmask_b32_e32 v117, v243, v117, vcc
	v_cmp_ne_u32_e32 vcc, 0, v232
	v_and_b32_e32 v232, 2, v223
	s_nop 0
	v_cndmask_b32_e32 v116, v243, v116, vcc
	v_cmp_ne_u32_e32 vcc, 0, v232
	v_and_b32_e32 v232, 1, v223
	s_nop 0
	v_cndmask_b32_e32 v115, v243, v115, vcc
	v_cmp_eq_u32_e32 vcc, 1, v232
	s_nop 1
	v_cndmask_b32_e32 v114, v243, v114, vcc
	s_setprio 1
	ds_read_b128 v[224:227], v211 offset:32768
	ds_read_b128 v[228:231], v211 offset:40960
	s_waitcnt lgkmcnt(1)
	v_mfma_f32_32x32x16_bf16 v[98:113], v[224:227], v[158:161], v[98:113]
	ds_read_b128 v[224:227], v212 offset:32768
	s_waitcnt lgkmcnt(1)
	v_mfma_f32_32x32x16_bf16 v[114:129], v[228:231], v[158:161], v[114:129]
	ds_read_b128 v[228:231], v212 offset:40960
	s_waitcnt lgkmcnt(1)
	v_mfma_f32_32x32x16_bf16 v[98:113], v[224:227], v[154:157], v[98:113]
	ds_read_b128 v[224:227], v213 offset:32768
	s_waitcnt lgkmcnt(1)
	v_mfma_f32_32x32x16_bf16 v[114:129], v[228:231], v[154:157], v[114:129]
	ds_read_b128 v[228:231], v213 offset:40960
	s_waitcnt lgkmcnt(1)
	v_mfma_f32_32x32x16_bf16 v[98:113], v[224:227], v[150:153], v[98:113]
	ds_read_b128 v[224:227], v214 offset:32768
	s_waitcnt lgkmcnt(1)
	v_mfma_f32_32x32x16_bf16 v[114:129], v[228:231], v[150:153], v[114:129]
	ds_read_b128 v[228:231], v214 offset:40960
	s_waitcnt lgkmcnt(1)
	v_mfma_f32_32x32x16_bf16 v[98:113], v[224:227], v[146:149], v[98:113]
	ds_read_b128 v[224:227], v211 offset:32896
	s_waitcnt lgkmcnt(1)
	v_mfma_f32_32x32x16_bf16 v[114:129], v[228:231], v[146:149], v[114:129]
	ds_read_b128 v[228:231], v211 offset:41088
	s_waitcnt lgkmcnt(1)
	v_mfma_f32_32x32x16_bf16 v[98:113], v[224:227], v[142:145], v[98:113]
	ds_read_b128 v[224:227], v212 offset:32896
	s_waitcnt lgkmcnt(1)
	v_mfma_f32_32x32x16_bf16 v[114:129], v[228:231], v[142:145], v[114:129]
	ds_read_b128 v[228:231], v212 offset:41088
	s_waitcnt lgkmcnt(1)
	v_mfma_f32_32x32x16_bf16 v[98:113], v[224:227], v[138:141], v[98:113]
	ds_read_b128 v[224:227], v213 offset:32896
	s_waitcnt lgkmcnt(1)
	v_mfma_f32_32x32x16_bf16 v[114:129], v[228:231], v[138:141], v[114:129]
	ds_read_b128 v[228:231], v213 offset:41088
	s_waitcnt lgkmcnt(1)
	v_mfma_f32_32x32x16_bf16 v[98:113], v[224:227], v[134:137], v[98:113]
	ds_read_b128 v[224:227], v214 offset:32896
	s_waitcnt lgkmcnt(1)
	v_mfma_f32_32x32x16_bf16 v[114:129], v[228:231], v[134:137], v[114:129]
	ds_read_b128 v[228:231], v214 offset:41088
	s_waitcnt lgkmcnt(1)
	v_mfma_f32_32x32x16_bf16 v[98:113], v[224:227], v[130:133], v[98:113]
	s_waitcnt lgkmcnt(0)
	v_mfma_f32_32x32x16_bf16 v[114:129], v[228:231], v[130:133], v[114:129]
	s_setprio 0
	s_add_i32 s55, s53, 1
	s_cmp_lt_u32 s55, s54
	s_cselect_b64 s[4:5], -1, 0
	s_cmp_ge_u32 s55, s54
	s_cbranch_scc1 .LBB0_1149
	global_load_dwordx2 v[196:197], v[194:195], off offset:8

.Lsw2_B:
	v_cndmask_b32_e64 v179, v222, v215, s[2:3]
	v_mul_f32_e32 v215, 0xbe0293ee, v179
	v_fmamk_f32 v66, v66, 0x3e0293ee, v215
	v_fmamk_f32 v67, v67, 0x3e0293ee, v215
	v_exp_f32_e32 v66, v66
	v_fmamk_f32 v68, v68, 0x3e0293ee, v215
	v_exp_f32_e32 v67, v67
	v_fmamk_f32 v69, v69, 0x3e0293ee, v215
	v_exp_f32_e32 v68, v68
	v_fmamk_f32 v70, v70, 0x3e0293ee, v215
	v_fmamk_f32 v82, v82, 0x3e0293ee, v215
	v_exp_f32_e32 v69, v69
	v_fmamk_f32 v71, v71, 0x3e0293ee, v215
	v_fmamk_f32 v72, v72, 0x3e0293ee, v215
	v_fmamk_f32 v73, v73, 0x3e0293ee, v215
	v_fmamk_f32 v74, v74, 0x3e0293ee, v215
	v_fmamk_f32 v75, v75, 0x3e0293ee, v215
	v_fmamk_f32 v76, v76, 0x3e0293ee, v215
	v_fmamk_f32 v77, v77, 0x3e0293ee, v215
	v_fmamk_f32 v78, v78, 0x3e0293ee, v215
	v_fmamk_f32 v79, v79, 0x3e0293ee, v215
	v_fmamk_f32 v80, v80, 0x3e0293ee, v215
	v_fmamk_f32 v81, v81, 0x3e0293ee, v215
	v_fmamk_f32 v83, v83, 0x3e0293ee, v215
	v_fmamk_f32 v84, v84, 0x3e0293ee, v215
	v_fmamk_f32 v85, v85, 0x3e0293ee, v215
	v_fmamk_f32 v86, v86, 0x3e0293ee, v215
	v_fmamk_f32 v87, v87, 0x3e0293ee, v215
	v_fmamk_f32 v88, v88, 0x3e0293ee, v215
	v_fmamk_f32 v89, v89, 0x3e0293ee, v215
	v_fmamk_f32 v90, v90, 0x3e0293ee, v215
	v_fmamk_f32 v91, v91, 0x3e0293ee, v215
	v_fmamk_f32 v92, v92, 0x3e0293ee, v215
	v_fmamk_f32 v93, v93, 0x3e0293ee, v215
	v_fmamk_f32 v94, v94, 0x3e0293ee, v215
	v_fmamk_f32 v95, v95, 0x3e0293ee, v215
	v_fmamk_f32 v96, v96, 0x3e0293ee, v215
	v_fmac_f32_e32 v215, 0x3e0293ee, v97
	v_exp_f32_e32 v70, v70
	v_exp_f32_e32 v97, v82
	v_add_f32_e32 v82, 0, v66
	v_exp_f32_e32 v71, v71
	v_add_f32_e32 v82, v67, v82
	v_exp_f32_e32 v72, v72
	v_add_f32_e32 v82, v68, v82
	v_exp_f32_e32 v73, v73
	v_add_f32_e32 v82, v69, v82
	v_exp_f32_e32 v74, v74
	v_add_f32_e32 v82, v70, v82
	v_exp_f32_e32 v75, v75
	v_add_f32_e32 v82, v71, v82
	v_exp_f32_e32 v76, v76
	v_add_f32_e32 v82, v72, v82
	v_exp_f32_e32 v77, v77
	v_add_f32_e32 v82, v73, v82
	v_exp_f32_e32 v78, v78
	v_add_f32_e32 v82, v74, v82
	v_exp_f32_e32 v79, v79
	v_add_f32_e32 v82, v75, v82
	v_exp_f32_e32 v80, v80
	v_add_f32_e32 v82, v76, v82
	v_exp_f32_e32 v81, v81
	v_add_f32_e32 v82, v77, v82
	v_add_f32_e32 v82, v78, v82
	v_exp_f32_e32 v222, v83
	v_add_f32_e32 v82, v79, v82
	v_exp_f32_e32 v84, v84
	v_add_f32_e32 v82, v80, v82
	v_exp_f32_e32 v85, v85
	v_add_f32_e32 v82, v81, v82
	v_exp_f32_e32 v86, v86
	v_add_f32_e32 v82, v97, v82
	v_exp_f32_e32 v87, v87
	v_add_f32_e32 v82, v222, v82
	v_exp_f32_e32 v88, v88
	v_add_f32_e32 v82, v84, v82
	v_exp_f32_e32 v89, v89
	v_add_f32_e32 v82, v85, v82
	v_exp_f32_e32 v90, v90
	v_add_f32_e32 v82, v86, v82
	v_exp_f32_e32 v91, v91
	v_add_f32_e32 v82, v87, v82
	v_exp_f32_e32 v92, v92
	v_add_f32_e32 v82, v88, v82
	v_exp_f32_e32 v93, v93
	v_add_f32_e32 v82, v89, v82
	v_exp_f32_e32 v94, v94
	v_add_f32_e32 v82, v90, v82
	v_exp_f32_e32 v95, v95
	v_add_f32_e32 v82, v91, v82
	v_exp_f32_e32 v96, v96
	v_add_f32_e32 v82, v92, v82
	v_exp_f32_e32 v215, v215
	v_add_f32_e32 v82, v93, v82
	v_add_f32_e32 v82, v94, v82
	v_add_f32_e32 v82, v95, v82
	v_add_f32_e32 v82, v96, v82
	v_add_f32_e32 v82, v215, v82
	v_mov_b32_e32 v83, v82
	v_cvt_pk_bf16_f32 v66, v66, v67
	v_cvt_pk_bf16_f32 v67, v68, v69
	v_cvt_pk_bf16_f32 v68, v70, v71
	v_cvt_pk_bf16_f32 v69, v72, v73
	v_cvt_pk_bf16_f32 v70, v74, v75
	v_cvt_pk_bf16_f32 v71, v76, v77
	v_cvt_pk_bf16_f32 v72, v78, v79
	v_cvt_pk_bf16_f32 v73, v80, v81
	v_cvt_pk_bf16_f32 v74, v97, v222
	v_cvt_pk_bf16_f32 v75, v84, v85
	v_cvt_pk_bf16_f32 v76, v86, v87
	v_cvt_pk_bf16_f32 v77, v88, v89
	v_cvt_pk_bf16_f32 v78, v90, v91
	v_cvt_pk_bf16_f32 v79, v92, v93
	v_cvt_pk_bf16_f32 v80, v94, v95
	v_cvt_pk_bf16_f32 v81, v96, v215
	s_nop 1
	v_permlane32_swap_b32_e32 v82, v83
	v_permlane32_swap_b32_e32 v66, v68
	v_permlane32_swap_b32_e32 v67, v69
	v_permlane32_swap_b32_e32 v70, v72
	v_permlane32_swap_b32_e32 v71, v73
	v_permlane32_swap_b32_e32 v74, v76
	v_permlane32_swap_b32_e32 v75, v77
	v_permlane32_swap_b32_e32 v78, v80
	v_permlane32_swap_b32_e32 v79, v81
	v_readlane_b32 vcc_lo, v255, 63
	s_bitcmp1_b32 vcc_lo, 0
	s_cbranch_scc1 .Lsw2_A
.Lsw2_done:
	v_cndmask_b32_e64 v84, 0, 1, s[4:5]
	v_cmp_ne_u32_e64 s[2:3], 1, v84
	s_andn2_b64 vcc, exec, s[4:5]
	s_cbranch_vccnz .LBB0_1151
	v_add_u32_e32 v88, 64, v217
	v_mad_i64_i32 v[84:85], s[4:5], v88, s84, v[190:191]
	v_add_u32_e32 v89, 0x60, v217
	v_mad_i64_i32 v[86:87], s[4:5], v89, s84, v[190:191]
	global_load_dwordx4 v[162:165], v[84:85], off
	global_load_dwordx4 v[166:169], v[86:87], off
	v_mad_i64_i32 v[84:85], s[4:5], v88, s84, v[192:193]
	v_mad_i64_i32 v[86:87], s[4:5], v89, s84, v[192:193]
	global_load_dwordx4 v[170:173], v[84:85], off
	global_load_dwordx4 v[174:177], v[86:87], off
